# baseline (speedup 1.0000x reference)
.LBB0_12:
	s_or_b64 exec, exec, s[4:5]
	v_mov_b32_e32 v29, 1
	s_waitcnt lgkmcnt(0)
	s_barrier
	ds_add_rtn_u32 v31, v35, v29
	ds_add_rtn_u32 v38, v34, v29
	ds_add_rtn_u32 v39, v30, v29
	ds_add_rtn_u32 v40, v28, v29
	ds_add_rtn_u32 v41, v27, v29
	s_mov_b32 s3, 0xff3c
	v_mad_u64_u32 v[32:33], s[4:5], v26, s3, v[12:13]
	v_lshl_or_b32 v12, v32, 16, v13
	v_mad_u64_u32 v[32:33], s[4:5], v25, s3, v[14:15]
	v_lshl_or_b32 v14, v32, 16, v15
	v_mad_u64_u32 v[32:33], s[4:5], v24, s3, v[16:17]
	v_lshl_or_b32 v16, v32, 16, v17
	v_mad_u64_u32 v[32:33], s[4:5], v23, s3, v[18:19]
	v_lshl_or_b32 v18, v32, 16, v19
	v_mad_u64_u32 v[32:33], s[4:5], v22, s3, v[20:21]
	v_lshl_or_b32 v20, v32, 16, v21
	v_lshl_add_u64 v[2:3], v[2:3], 2, s[6:7]
	v_lshl_add_u64 v[4:5], v[4:5], 2, s[6:7]
	s_mov_b64 s[4:5], 0
	s_waitcnt lgkmcnt(4)
	v_lshlrev_b32_e32 v13, 2, v31
	ds_write_b32 v13, v12
	s_waitcnt lgkmcnt(4)
	v_lshlrev_b32_e32 v13, 2, v38
	ds_write_b32 v13, v14
	s_waitcnt lgkmcnt(4)
	v_lshlrev_b32_e32 v13, 2, v39
	ds_write_b32 v13, v16
	s_waitcnt lgkmcnt(4)
	v_lshlrev_b32_e32 v13, 2, v40
	ds_write_b32 v13, v18
	s_waitcnt lgkmcnt(4)
	v_lshlrev_b32_e32 v13, 2, v41
	ds_write_b32 v13, v20
	s_waitcnt lgkmcnt(0)
	s_barrier
	ds_read2st64_b32 v[12:13], v1 offset1:16
	s_waitcnt lgkmcnt(0)
	global_store_dword v[2:3], v12, off sc0 sc1
	ds_read2st64_b32 v[2:3], v1 offset0:32 offset1:48
	ds_read_b32 v1, v1 offset:16384
	global_store_dword v[4:5], v13, off sc0 sc1
	v_lshl_add_u64 v[4:5], v[6:7], 2, s[6:7]
	s_waitcnt lgkmcnt(1)
	global_store_dword v[4:5], v2, off sc0 sc1
	v_lshl_add_u64 v[4:5], v[8:9], 2, s[6:7]
	global_store_dword v[4:5], v3, off sc0 sc1
	v_lshl_add_u64 v[2:3], v[10:11], 2, s[6:7]
	s_waitcnt lgkmcnt(0)
	global_store_dword v[2:3], v1, off sc0 sc1

	.amdhsa_kernel _Z11k_chunksortPKiS0_PjS1_PKfS3_S3_S3_S3_PDF16_S4_PfS5_S4_Ph
		.amdhsa_group_segment_fixed_size 21520
		.amdhsa_private_segment_fixed_size 0
		.amdhsa_kernarg_size 376
		.amdhsa_user_sgpr_count 2
		.amdhsa_user_sgpr_dispatch_ptr 0
		.amdhsa_user_sgpr_queue_ptr 0
		.amdhsa_user_sgpr_kernarg_segment_ptr 1
		.amdhsa_user_sgpr_dispatch_id 0
		.amdhsa_user_sgpr_kernarg_preload_length 0
		.amdhsa_user_sgpr_kernarg_preload_offset 0
		.amdhsa_user_sgpr_private_segment_size 0
		.amdhsa_uses_dynamic_stack 0
		.amdhsa_enable_private_segment 0
		.amdhsa_system_sgpr_workgroup_id_x 1
		.amdhsa_system_sgpr_workgroup_id_y 0
		.amdhsa_system_sgpr_workgroup_id_z 0
		.amdhsa_system_sgpr_workgroup_info 0
		.amdhsa_system_vgpr_workitem_id 0
		.amdhsa_next_free_vgpr 48
		.amdhsa_next_free_sgpr 26
		.amdhsa_accum_offset 48
		.amdhsa_reserve_vcc 1
		.amdhsa_float_round_mode_32 0
		.amdhsa_float_round_mode_16_64 0
		.amdhsa_float_denorm_mode_32 3
		.amdhsa_float_denorm_mode_16_64 3
		.amdhsa_dx10_clamp 1
		.amdhsa_ieee_mode 1
		.amdhsa_fp16_overflow 0
		.amdhsa_tg_split 0
		.amdhsa_exception_fp_ieee_invalid_op 0
		.amdhsa_exception_fp_denorm_src 0
		.amdhsa_exception_fp_ieee_div_zero 0
		.amdhsa_exception_fp_ieee_overflow 0
		.amdhsa_exception_fp_ieee_underflow 0
		.amdhsa_exception_fp_ieee_inexact 0
		.amdhsa_exception_int_div_zero 0
	.end_amdhsa_kernel

amdhsa.kernels:
  - .agpr_count:     0
    .args:
      - .actual_access:  read_only
        .address_space:  global
        .offset:         0
        .size:           8
        .value_kind:     global_buffer
      - .actual_access:  read_only
        .address_space:  global
        .offset:         8
        .size:           8
        .value_kind:     global_buffer
      - .actual_access:  write_only
        .address_space:  global
        .offset:         16
        .size:           8
        .value_kind:     global_buffer
      - .actual_access:  write_only
        .address_space:  global
        .offset:         24
        .size:           8
        .value_kind:     global_buffer
      - .actual_access:  read_only
        .address_space:  global
        .offset:         32
        .size:           8
        .value_kind:     global_buffer
      - .actual_access:  read_only
        .address_space:  global
        .offset:         40
        .size:           8
        .value_kind:     global_buffer
      - .actual_access:  read_only
        .address_space:  global
        .offset:         48
        .size:           8
        .value_kind:     global_buffer
      - .actual_access:  read_only
        .address_space:  global
        .offset:         56
        .size:           8
        .value_kind:     global_buffer
      - .actual_access:  read_only
        .address_space:  global
        .offset:         64
        .size:           8
        .value_kind:     global_buffer
      - .actual_access:  write_only
        .address_space:  global
        .offset:         72
        .size:           8
        .value_kind:     global_buffer
      - .actual_access:  write_only
        .address_space:  global
        .offset:         80
        .size:           8
        .value_kind:     global_buffer
      - .actual_access:  write_only
        .address_space:  global
        .offset:         88
        .size:           8
        .value_kind:     global_buffer
      - .actual_access:  write_only
        .address_space:  global
        .offset:         96
        .size:           8
        .value_kind:     global_buffer
      - .actual_access:  write_only
        .address_space:  global
        .offset:         104
        .size:           8
        .value_kind:     global_buffer
      - .actual_access:  write_only
        .address_space:  global
        .offset:         112
        .size:           8
        .value_kind:     global_buffer
      - .offset:         120
        .size:           4
        .value_kind:     hidden_block_count_x
      - .offset:         124
        .size:           4
        .value_kind:     hidden_block_count_y
      - .offset:         128
        .size:           4
        .value_kind:     hidden_block_count_z
      - .offset:         132
        .size:           2
        .value_kind:     hidden_group_size_x
      - .offset:         134
        .size:           2
        .value_kind:     hidden_group_size_y
      - .offset:         136
        .size:           2
        .value_kind:     hidden_group_size_z
      - .offset:         138
        .size:           2
        .value_kind:     hidden_remainder_x
      - .offset:         140
        .size:           2
        .value_kind:     hidden_remainder_y
      - .offset:         142
        .size:           2
        .value_kind:     hidden_remainder_z
      - .offset:         160
        .size:           8
        .value_kind:     hidden_global_offset_x
      - .offset:         168
        .size:           8
        .value_kind:     hidden_global_offset_y
      - .offset:         176
        .size:           8
        .value_kind:     hidden_global_offset_z
      - .offset:         184
        .size:           2
        .value_kind:     hidden_grid_dims
    .group_segment_fixed_size: 21520
    .kernarg_segment_align: 8
    .kernarg_segment_size: 376
    .language:       OpenCL C
    .language_version:
      - 2
      - 0
    .max_flat_workgroup_size: 1024
    .name:           _Z11k_chunksortPKiS0_PjS1_PKfS3_S3_S3_S3_PDF16_S4_PfS5_S4_Ph
    .private_segment_fixed_size: 0
    .sgpr_count:     32
    .sgpr_spill_count: 0
    .symbol:         _Z11k_chunksortPKiS0_PjS1_PKfS3_S3_S3_S3_PDF16_S4_PfS5_S4_Ph.kd
    .uniform_work_group_size: 1
    .uses_dynamic_stack: false
    .vgpr_count:     48
    .vgpr_spill_count: 0
    .wavefront_size: 64
  - .agpr_count:     0
    .args:
      - .actual_access:  read_only
        .address_space:  global
        .offset:         0
        .size:           8
        .value_kind:     global_buffer
      - .actual_access:  read_only
        .address_space:  global
        .offset:         8
        .size:           8
        .value_kind:     global_buffer
      - .actual_access:  read_only
        .address_space:  global
        .offset:         16
        .size:           8
        .value_kind:     global_buffer
      - .actual_access:  write_only
        .address_space:  global
        .offset:         24
        .size:           8
        .value_kind:     global_buffer
      - .actual_access:  write_only
        .address_space:  global
        .offset:         32
        .size:           8
        .value_kind:     global_buffer
      - .actual_access:  write_only
        .address_space:  global
        .offset:         40
        .size:           8
        .value_kind:     global_buffer
      - .actual_access:  write_only
        .address_space:  global
        .offset:         48
        .size:           8
        .value_kind:     global_buffer
    .group_segment_fixed_size: 22536
    .kernarg_segment_align: 8
    .kernarg_segment_size: 56
    .language:       OpenCL C
    .language_version:
      - 2
      - 0
    .max_flat_workgroup_size: 1024
    .name:           _Z5k_csrPKjS0_PKfPjPfPDF16_P15HIP_vector_typeIjLj4EE
    .private_segment_fixed_size: 0
    .sgpr_count:     54
    .sgpr_spill_count: 0
    .symbol:         _Z5k_csrPKjS0_PKfPjPfPDF16_P15HIP_vector_typeIjLj4EE.kd
    .uniform_work_group_size: 1
    .uses_dynamic_stack: false
    .vgpr_count:     64
    .vgpr_spill_count: 0
    .wavefront_size: 64
  - .agpr_count:     0
    .args:
      - .actual_access:  read_only
        .address_space:  global
        .offset:         0
        .size:           8
        .value_kind:     global_buffer
      - .actual_access:  read_only
        .address_space:  global
        .offset:         8
        .size:           8
        .value_kind:     global_buffer
      - .actual_access:  read_only
        .address_space:  global
        .offset:         16
        .size:           8
        .value_kind:     global_buffer
      - .actual_access:  read_only
        .address_space:  global
        .offset:         24
        .size:           8
        .value_kind:     global_buffer
      - .actual_access:  read_only
        .address_space:  global
        .offset:         32
        .size:           8
        .value_kind:     global_buffer
      - .actual_access:  read_only
        .address_space:  global
        .offset:         40
        .size:           8
        .value_kind:     global_buffer
      - .actual_access:  read_only
        .address_space:  global
        .offset:         48
        .size:           8
        .value_kind:     global_buffer
      - .actual_access:  write_only
        .address_space:  global
        .offset:         56
        .size:           8
        .value_kind:     global_buffer
      - .actual_access:  write_only
        .address_space:  global
        .offset:         64
        .size:           8
        .value_kind:     global_buffer
    .group_segment_fixed_size: 36112
    .kernarg_segment_align: 8
    .kernarg_segment_size: 72
    .language:       OpenCL C
    .language_version:
      - 2
      - 0
    .max_flat_workgroup_size: 256
    .name:           _Z8k_layer1PKfPKDF16_PK15HIP_vector_typeIjLj4EEPKjS0_S2_S0_PhPf
    .private_segment_fixed_size: 0
    .sgpr_count:     30
    .sgpr_spill_count: 0
    .symbol:         _Z8k_layer1PKfPKDF16_PK15HIP_vector_typeIjLj4EEPKjS0_S2_S0_PhPf.kd
    .uniform_work_group_size: 1
    .uses_dynamic_stack: false
    .vgpr_count:     128
    .vgpr_spill_count: 0
    .wavefront_size: 64
  - .agpr_count:     0
    .args:
      - .actual_access:  read_only
        .address_space:  global
        .offset:         0
        .size:           8
        .value_kind:     global_buffer
      - .actual_access:  read_only
        .address_space:  global
        .offset:         8
        .size:           8
        .value_kind:     global_buffer
      - .actual_access:  read_only
        .address_space:  global
        .offset:         16
        .size:           8
        .value_kind:     global_buffer
      - .actual_access:  read_only
        .address_space:  global
        .offset:         24
        .size:           8
        .value_kind:     global_buffer
      - .actual_access:  read_only
        .address_space:  global
        .offset:         32
        .size:           8
        .value_kind:     global_buffer
      - .actual_access:  read_only
        .address_space:  global
        .offset:         40
        .size:           8
        .value_kind:     global_buffer
      - .actual_access:  read_only
        .address_space:  global
        .offset:         48
        .size:           8
        .value_kind:     global_buffer
      - .address_space:  global
        .offset:         56
        .size:           8
        .value_kind:     global_buffer
    .group_segment_fixed_size: 39168
    .kernarg_segment_align: 8
    .kernarg_segment_size: 64
    .language:       OpenCL C
    .language_version:
      - 2
      - 0
    .max_flat_workgroup_size: 256
    .name:           _Z8k_layer2PKhPKfPK15HIP_vector_typeIjLj4EEPKjS2_PKDF16_S2_Pf
    .private_segment_fixed_size: 0
    .sgpr_count:     27
    .sgpr_spill_count: 0
    .symbol:         _Z8k_layer2PKhPKfPK15HIP_vector_typeIjLj4EEPKjS2_PKDF16_S2_Pf.kd
    .uniform_work_group_size: 1
    .uses_dynamic_stack: false
    .vgpr_count:     112
    .vgpr_spill_count: 0
    .wavefront_size: 64
  - .agpr_count:     0
    .args:
      - .actual_access:  read_only
        .address_space:  global
        .offset:         0
        .size:           8
        .value_kind:     global_buffer
      - .actual_access:  read_only
        .address_space:  global
        .offset:         8
        .size:           8
        .value_kind:     global_buffer
      - .actual_access:  read_only
        .address_space:  global
        .offset:         16
        .size:           8
        .value_kind:     global_buffer
      - .actual_access:  read_only
        .address_space:  global
        .offset:         24
        .size:           8
        .value_kind:     global_buffer
      - .actual_access:  read_only
        .address_space:  global
        .offset:         32
        .size:           8
        .value_kind:     global_buffer
      - .actual_access:  write_only
        .address_space:  global
        .offset:         40
        .size:           8
        .value_kind:     global_buffer
    .group_segment_fixed_size: 512
    .kernarg_segment_align: 8
    .kernarg_segment_size: 48
    .language:       OpenCL C
    .language_version:
      - 2
      - 0
    .max_flat_workgroup_size: 320
    .name:           _Z7k_headsPKfS0_S0_S0_S0_Pf
    .private_segment_fixed_size: 0
    .sgpr_count:     22
    .sgpr_spill_count: 0
    .symbol:         _Z7k_headsPKfS0_S0_S0_S0_Pf.kd
    .uniform_work_group_size: 1
    .uses_dynamic_stack: false
    .vgpr_count:     56
    .vgpr_spill_count: 0
    .wavefront_size: 64
